# per_light 12->22 gu, 7->14 down; plus S5 epilogue hoist, dead S5 disc removed
# speedup vs baseline: 1.0240x; 1.0184x over previous
; __device__ __forceinline__ void conv_slice(const Ctx& c, int lo0, int n0, int lo1, int n1, int lo2, int n2) {
;     const int tot = n0 + n1 + n2, G = c.G;
;     const int mine = (tot - c.bid + G - 1) / G;
;     if (mine <= 0) return;
;     const int tid = c.tid, w = c.wave, lrow = c.lane >> 5, gp = c.lane & 31;
;     const int rr0 = tid >> 3, kq = tid & 7;
; __device__ __forceinline__ void conv_slice_moe(const Ctx& c, int lo, int n, int nwg, int per_light) {
;     const int extra = nwg % c.G, n_light = extra ? c.G - extra : 0;
;     int nb = n_light * per_light; if (nb > n) nb = n;
;     if (n_light > 0 && c.bid >= extra && nb > 0) { Ctx c2 = c; c2.bid = c.bid - extra; c2.G = n_light; conv_slice(c2, lo, nb, 0, 0, 0, 0); }
;     conv_slice(c, lo + nb, n - nb, 0, 0, 0, 0);
.LBB0_853:
	s_abs_i32 s30, s96
	v_cvt_f32_u32_e32 v0, s30
	s_sub_i32 s1, 0, s30
	s_abs_i32 s0, s12
	s_ashr_i32 s13, s12, 31
	v_rcp_iflag_f32_e32 v0, v0
	s_ashr_i32 s31, s96, 31
	v_mul_f32_e32 v0, 0x4f7ffffe, v0
	v_cvt_u32_f32_e32 v0, v0
	s_nop 0
	v_readfirstlane_b32 s34, v0
	s_mul_i32 s1, s1, s34
	s_mul_hi_u32 s1, s34, s1
	s_add_i32 s34, s34, s1
	s_mul_hi_u32 s1, s0, s34
	s_mul_i32 s1, s1, s30
	s_sub_i32 s0, s0, s1
	s_sub_i32 s1, s0, s30
	s_cmp_ge_u32 s0, s30
	s_cselect_b32 s0, s1, s0
	s_sub_i32 s1, s0, s30
	s_cmp_ge_u32 s0, s30
	s_cselect_b32 s0, s1, s0
	s_xor_b32 s0, s0, s13
	s_sub_i32 s1, s0, s13
	s_sub_i32 s0, s96, s1
	s_cmp_lg_u32 s1, 0
	s_cselect_b32 s35, s0, 0
	s_mul_i32 s4, s35, 22
	s_min_i32 s33, s4, 0x1000
	s_cmp_lt_i32 s35, 1
	s_cselect_b64 s[4:5], -1, 0
	s_cmp_lt_i32 s2, s1
	s_cselect_b64 s[6:7], -1, 0
	s_or_b64 s[4:5], s[4:5], s[6:7]
	s_and_b64 vcc, exec, s[4:5]
	s_cbranch_vccnz .LBB0_959
	s_abs_i32 s4, s0
	v_cvt_f32_u32_e32 v0, s4
	s_sub_i32 s59, s2, s1
	s_not_b32 s1, s59
	s_sub_i32 s5, 0, s4
	v_rcp_iflag_f32_e32 v0, v0
	s_add_i32 s1, s0, s1
	s_add_i32 s1, s1, s33
	s_xor_b32 s0, s1, s0
	v_mul_f32_e32 v0, 0x4f7ffffe, v0
	v_cvt_u32_f32_e32 v0, v0
	s_abs_i32 s1, s1
	s_ashr_i32 s0, s0, 31
	v_readfirstlane_b32 s6, v0
	s_mul_i32 s5, s5, s6
	s_mul_hi_u32 s5, s6, s5
	s_add_i32 s6, s6, s5
	s_mul_hi_u32 s5, s1, s6
	s_mul_i32 s6, s5, s4
	s_sub_i32 s1, s1, s6
	s_add_i32 s7, s5, 1
	s_sub_i32 s6, s1, s4
	s_cmp_ge_u32 s1, s4
	s_cselect_b32 s5, s7, s5
	s_cselect_b32 s1, s6, s1
	s_add_i32 s6, s5, 1
	s_cmp_ge_u32 s1, s4
	s_cselect_b32 s1, s6, s5
	s_xor_b32 s1, s1, s0
	s_sub_i32 s37, s1, s0
	s_cmp_lt_i32 s37, 1
	s_cbranch_scc1 .LBB0_959
	s_sub_i32 s38, 0, s33
	s_cmp_ge_i32 s59, s33
	s_cselect_b32 s7, s38, 0x4680
	s_add_i32 s7, s7, s59
	s_cmpk_gt_i32 s7, 0x37f
	s_cbranch_scc0 .LBB0_860
	s_cmpk_gt_u32 s7, 0x47f
	s_cbranch_scc0 .LBB0_861
	s_cmpk_gt_u32 s7, 0x67f
	s_cbranch_scc0 .LBB0_862
	s_cmpk_gt_u32 s7, 0x467f
	s_cbranch_scc0 .LBB0_863
	s_add_i32 s0, s7, 0xffffb980
	s_lshr_b32 s0, s0, 7
	s_mov_b32 s1, 0
	s_lshl_b64 s[0:1], s[0:1], 23
	v_readlane_b32 s20, v254, 0
	v_readlane_b32 s21, v254, 1
	s_add_u32 s4, s20, s0
	s_addc_u32 s5, s21, s1
	s_lshl_b32 s0, s7, 7
	s_and_b32 s26, s0, 0x380
	s_lshl_b32 s0, s7, 4
	v_readlane_b32 s22, v254, 2
	v_readlane_b32 s23, v254, 3
	s_and_b32 s6, s0, 0x780
	s_mov_b64 s[0:1], 0
	s_branch .LBB0_864

; __device__ __forceinline__ void conv_slice(const Ctx& c, int lo0, int n0, int lo1, int n1, int lo2, int n2) {
;     const int tot = n0 + n1 + n2, G = c.G;
;     const int mine = (tot - c.bid + G - 1) / G;
;     if (mine <= 0) return;
;     const int tid = c.tid, w = c.wave, lrow = c.lane >> 5, gp = c.lane & 31;
;     const int rr0 = tid >> 3, kq = tid & 7;
; __device__ __forceinline__ void conv_slice_moe(const Ctx& c, int lo, int n, int nwg, int per_light) {
;     const int extra = nwg % c.G, n_light = extra ? c.G - extra : 0;
;     int nb = n_light * per_light; if (nb > n) nb = n;
;     if (n_light > 0 && c.bid >= extra && nb > 0) { Ctx c2 = c; c2.bid = c.bid - extra; c2.G = n_light; conv_slice(c2, lo, nb, 0, 0, 0, 0); }
;     conv_slice(c, lo + nb, n - nb, 0, 0, 0, 0);
.LBB0_1217:
	s_abs_i32 s33, s96
	v_cvt_f32_u32_e32 v0, s33
	s_sub_i32 s1, 0, s33
	s_abs_i32 s0, s6
	s_ashr_i32 s7, s6, 31
	v_rcp_iflag_f32_e32 v0, v0
	s_ashr_i32 s41, s96, 31
	v_mul_f32_e32 v0, 0x4f7ffffe, v0
	v_cvt_u32_f32_e32 v0, v0
	s_nop 0
	v_readfirstlane_b32 s43, v0
	s_mul_i32 s1, s1, s43
	s_mul_hi_u32 s1, s43, s1
	s_add_i32 s43, s43, s1
	s_mul_hi_u32 s1, s0, s43
	s_mul_i32 s1, s1, s33
	s_sub_i32 s0, s0, s1
	s_sub_i32 s1, s0, s33
	s_cmp_ge_u32 s0, s33
	s_cselect_b32 s0, s1, s0
	s_sub_i32 s1, s0, s33
	s_cmp_ge_u32 s0, s33
	s_cselect_b32 s0, s1, s0
	s_xor_b32 s0, s0, s7
	s_sub_i32 s1, s0, s7
	s_sub_i32 s0, s96, s1
	s_cmp_lg_u32 s1, 0
	s_cselect_b32 s44, s0, 0
	s_mul_i32 s12, s44, 14
	s_min_i32 s42, s12, 0xd00
	s_cmp_lt_i32 s44, 1
	s_cselect_b64 s[12:13], -1, 0
	s_cmp_lt_i32 s2, s1
	s_cselect_b64 s[14:15], -1, 0
	s_or_b64 s[12:13], s[12:13], s[14:15]
	s_and_b64 vcc, exec, s[12:13]
	s_cbranch_vccnz .LBB0_1322
	s_abs_i32 s12, s0
	v_cvt_f32_u32_e32 v0, s12
	s_sub_i32 s45, s2, s1
	s_not_b32 s1, s45
	s_sub_i32 s13, 0, s12
	v_rcp_iflag_f32_e32 v0, v0
	s_add_i32 s1, s0, s1
	s_add_i32 s1, s1, s42
	s_xor_b32 s0, s1, s0
	v_mul_f32_e32 v0, 0x4f7ffffe, v0
	v_cvt_u32_f32_e32 v0, v0
	s_abs_i32 s1, s1
	s_ashr_i32 s0, s0, 31
	v_readfirstlane_b32 s14, v0
	s_mul_i32 s13, s13, s14
	s_mul_hi_u32 s13, s14, s13
	s_add_i32 s14, s14, s13
	s_mul_hi_u32 s13, s1, s14
	s_mul_i32 s14, s13, s12
	s_sub_i32 s1, s1, s14
	s_add_i32 s15, s13, 1
	s_sub_i32 s14, s1, s12
	s_cmp_ge_u32 s1, s12
	s_cselect_b32 s13, s15, s13
	s_cselect_b32 s1, s14, s1
	s_add_i32 s14, s13, 1
	s_cmp_ge_u32 s1, s12
	s_cselect_b32 s1, s14, s13
	s_xor_b32 s1, s1, s0
	s_sub_i32 s48, s1, s0
	s_cmp_lt_i32 s48, 1
	s_cbranch_scc1 .LBB0_1322
	s_sub_i32 s49, 0, s42
	s_cmp_ge_i32 s45, s42
	s_cselect_b32 s15, s49, 0x2680
	s_add_i32 s15, s15, s45
	s_cmpk_gt_i32 s15, 0x37f
	s_cbranch_scc0 .LBB0_1224
	v_readlane_b32 s52, v254, 47
	s_cmpk_gt_u32 s15, 0x47f
	v_readlane_b32 s53, v254, 48
	v_readlane_b32 s54, v254, 49
	v_readlane_b32 s55, v254, 50
	v_readlane_b32 s56, v254, 51
	v_readlane_b32 s57, v254, 52
	v_readlane_b32 s58, v254, 53
	v_readlane_b32 s59, v254, 54
	v_readlane_b32 s60, v254, 55
	v_readlane_b32 s61, v254, 56
	v_readlane_b32 s62, v254, 57
	v_readlane_b32 s63, v254, 58
	v_readlane_b32 s64, v254, 59
	v_readlane_b32 s65, v254, 60
	v_readlane_b32 s66, v254, 61
	v_readlane_b32 s67, v254, 62
	s_cbranch_scc0 .LBB0_1225
	s_cmpk_gt_u32 s15, 0x67f
	s_cbranch_scc0 .LBB0_1226
	s_cmpk_gt_u32 s15, 0x467f
	s_cbranch_scc0 .LBB0_1227
	s_add_i32 s0, s15, 0xffffb980
	s_lshr_b32 s0, s0, 7
	s_mov_b32 s1, 0
	s_lshl_b64 s[0:1], s[0:1], 23
	v_readlane_b32 s16, v254, 0
	v_readlane_b32 s17, v254, 1
	s_add_u32 s12, s16, s0
	s_addc_u32 s13, s17, s1
	s_lshl_b32 s0, s15, 7
	s_and_b32 s24, s0, 0x380
	s_lshl_b32 s0, s15, 4
	v_readlane_b32 s18, v254, 2
	v_readlane_b32 s19, v254, 3
	s_and_b32 s14, s0, 0x780
	s_mov_b64 s[0:1], 0
	s_branch .LBB0_1228

; __device__ __forceinline__ void conv_slice(const Ctx& c, int lo0, int n0, int lo1, int n1, int lo2, int n2) {
;     const int tot = n0 + n1 + n2, G = c.G;
;     const int mine = (tot - c.bid + G - 1) / G;
;     if (mine <= 0) return;
;     const int tid = c.tid, w = c.wave, lrow = c.lane >> 5, gp = c.lane & 31;
;     const int rr0 = tid >> 3, kq = tid & 7;
; __device__ __forceinline__ void conv_slice_moe(const Ctx& c, int lo, int n, int nwg, int per_light) {
;     const int extra = nwg % c.G, n_light = extra ? c.G - extra : 0;
;     int nb = n_light * per_light; if (nb > n) nb = n;
;     if (n_light > 0 && c.bid >= extra && nb > 0) { Ctx c2 = c; c2.bid = c.bid - extra; c2.G = n_light; conv_slice(c2, lo, nb, 0, 0, 0, 0); }
;     conv_slice(c, lo + nb, n - nb, 0, 0, 0, 0);
.LBB0_2182:
	s_abs_i32 s30, s96
	v_cvt_f32_u32_e32 v0, s30
	s_sub_i32 s1, 0, s30
	s_abs_i32 s0, s12
	s_ashr_i32 s13, s12, 31
	v_rcp_iflag_f32_e32 v0, v0
	s_ashr_i32 s31, s96, 31
	v_mul_f32_e32 v0, 0x4f7ffffe, v0
	v_cvt_u32_f32_e32 v0, v0
	s_nop 0
	v_readfirstlane_b32 s34, v0
	s_mul_i32 s1, s1, s34
	s_mul_hi_u32 s1, s34, s1
	s_add_i32 s34, s34, s1
	s_mul_hi_u32 s1, s0, s34
	s_mul_i32 s1, s1, s30
	s_sub_i32 s0, s0, s1
	s_sub_i32 s1, s0, s30
	s_cmp_ge_u32 s0, s30
	s_cselect_b32 s0, s1, s0
	s_sub_i32 s1, s0, s30
	s_cmp_ge_u32 s0, s30
	s_cselect_b32 s0, s1, s0
	s_xor_b32 s0, s0, s13
	s_sub_i32 s1, s0, s13
	s_sub_i32 s0, s96, s1
	s_cmp_lg_u32 s1, 0
	s_cselect_b32 s35, s0, 0
	s_mul_i32 s4, s35, 22
	s_min_i32 s33, s4, 0x1000
	s_cmp_lt_i32 s35, 1
	s_cselect_b64 s[4:5], -1, 0
	s_cmp_lt_i32 s2, s1
	s_cselect_b64 s[6:7], -1, 0
	s_or_b64 s[4:5], s[4:5], s[6:7]
	s_and_b64 vcc, exec, s[4:5]
	s_cbranch_vccnz .LBB0_2287
	s_abs_i32 s4, s0
	v_cvt_f32_u32_e32 v0, s4
	s_sub_i32 s36, s2, s1
	s_not_b32 s1, s36
	s_sub_i32 s5, 0, s4
	v_rcp_iflag_f32_e32 v0, v0
	s_add_i32 s1, s0, s1
	s_add_i32 s1, s1, s33
	s_xor_b32 s0, s1, s0
	v_mul_f32_e32 v0, 0x4f7ffffe, v0
	v_cvt_u32_f32_e32 v0, v0
	s_abs_i32 s1, s1
	s_ashr_i32 s0, s0, 31
	v_readfirstlane_b32 s6, v0
	s_mul_i32 s5, s5, s6
	s_mul_hi_u32 s5, s6, s5
	s_add_i32 s6, s6, s5
	s_mul_hi_u32 s5, s1, s6
	s_mul_i32 s6, s5, s4
	s_sub_i32 s1, s1, s6
	s_add_i32 s7, s5, 1
	s_sub_i32 s6, s1, s4
	s_cmp_ge_u32 s1, s4
	s_cselect_b32 s5, s7, s5
	s_cselect_b32 s1, s6, s1
	s_add_i32 s6, s5, 1
	s_cmp_ge_u32 s1, s4
	s_cselect_b32 s1, s6, s5
	s_xor_b32 s1, s1, s0
	s_sub_i32 s37, s1, s0
	s_cmp_lt_i32 s37, 1
	s_cbranch_scc1 .LBB0_2287
	s_sub_i32 s38, 0, s33
	s_cmp_ge_i32 s36, s33
	s_cselect_b32 s7, s38, 0x5680
	s_add_i32 s7, s7, s36
	s_cmpk_gt_i32 s7, 0x37f
	s_cbranch_scc0 .LBB0_2189
	v_readlane_b32 s56, v254, 47
	s_cmpk_gt_u32 s7, 0x47f
	v_readlane_b32 s57, v254, 48
	v_readlane_b32 s58, v254, 49
	v_readlane_b32 s59, v254, 50
	v_readlane_b32 s60, v254, 51
	v_readlane_b32 s61, v254, 52
	v_readlane_b32 s62, v254, 53
	v_readlane_b32 s63, v254, 54
	v_readlane_b32 s64, v254, 55
	v_readlane_b32 s65, v254, 56
	v_readlane_b32 s66, v254, 57
	v_readlane_b32 s67, v254, 58
	v_readlane_b32 s68, v254, 59
	v_readlane_b32 s69, v254, 60
	v_readlane_b32 s70, v254, 61
	v_readlane_b32 s71, v254, 62
	s_cbranch_scc0 .LBB0_2190
	s_cmpk_gt_u32 s7, 0x67f
	s_cbranch_scc0 .LBB0_2191
	s_cmpk_gt_u32 s7, 0x467f
	s_cbranch_scc0 .LBB0_2192
	s_add_i32 s0, s7, 0xffffb980
	s_lshr_b32 s0, s0, 7
	s_mov_b32 s1, 0
	s_lshl_b64 s[0:1], s[0:1], 23
	v_readlane_b32 s20, v254, 0
	v_readlane_b32 s21, v254, 1
	s_add_u32 s4, s20, s0
	s_addc_u32 s5, s21, s1
	s_lshl_b32 s0, s7, 7
	s_and_b32 s26, s0, 0x380
	s_lshl_b32 s0, s7, 4
	v_readlane_b32 s22, v254, 2
	v_readlane_b32 s23, v254, 3
	s_and_b32 s6, s0, 0x780
	s_mov_b64 s[0:1], 0
	s_branch .LBB0_2193
